# baseline (speedup 1.0000x reference)
_Z2kBPKfPKDv4_jPKDF16_S0_S0_S0_Pf:
	v_lshrrev_b32_e32 v11, 7, v0
	s_load_dwordx8 s[4:11], s[0:1], 0x0
	s_load_dwordx4 s[12:15], s[0:1], 0x20
	s_load_dwordx2 s[16:17], s[0:1], 0x30
	v_lshl_or_b32 v2, s2, 2, v11
	s_mov_b32 s2, 0x4ec4ec4f
	v_mul_hi_i32 v1, v2, s2
	v_lshrrev_b32_e32 v3, 31, v1
	v_ashrrev_i32_e32 v1, 2, v1
	v_add_u32_e32 v1, v1, v3
	v_and_b32_e32 v108, 15, v0
	v_mad_u64_u32 v[4:5], s[2:3], v1, -13, v[2:3]
	v_lshlrev_b32_e32 v102, 4, v0
	v_mov_b32_e32 v103, 0
	v_lshl_or_b32 v10, v4, 4, v108
	s_waitcnt lgkmcnt(0)
	v_lshl_add_u64 v[4:5], s[8:9], 0, v[102:103]
	s_movk_i32 s2, 0x2000
	v_add_co_u32_e32 v6, vcc, s2, v4
	s_movk_i32 s2, 0x4000
	s_nop 0
	v_addc_co_u32_e32 v7, vcc, 0, v5, vcc
	v_add_co_u32_e32 v8, vcc, s2, v4
	s_movk_i32 s2, 0x6000
	s_nop 0
	v_addc_co_u32_e32 v9, vcc, 0, v5, vcc
	global_load_dwordx4 v[14:17], v102, s[8:9]
	global_load_dwordx4 v[18:21], v[6:7], off
	global_load_dwordx4 v[22:25], v[8:9], off
	v_add_co_u32_e32 v6, vcc, s2, v4
	s_mov_b32 s2, 0x8000
	s_nop 0
	v_addc_co_u32_e32 v7, vcc, 0, v5, vcc
	v_add_co_u32_e32 v8, vcc, s2, v4
	s_mov_b32 s2, 0xa000
	s_nop 0
	v_addc_co_u32_e32 v9, vcc, 0, v5, vcc
	global_load_dwordx4 v[26:29], v[6:7], off
	global_load_dwordx4 v[30:33], v[8:9], off
	v_add_co_u32_e32 v6, vcc, s2, v4
	s_mov_b32 s2, 0xc000
	s_nop 0
	v_addc_co_u32_e32 v7, vcc, 0, v5, vcc
	v_add_co_u32_e32 v8, vcc, s2, v4
	s_mov_b32 s2, 0xe000
	s_nop 0
	v_addc_co_u32_e32 v9, vcc, 0, v5, vcc
	v_add_co_u32_e32 v4, vcc, s2, v4
	s_movk_i32 s2, 0xc8
	s_nop 0
	v_addc_co_u32_e32 v5, vcc, 0, v5, vcc
	global_load_dwordx4 v[34:37], v[6:7], off
	global_load_dwordx4 v[38:41], v[8:9], off
	v_mov_b32_e32 v3, 0xc7
	v_cmp_gt_i32_e32 vcc, s2, v10
	global_load_dwordx4 v[42:45], v[4:5], off
	s_movk_i32 s2, 0x320
	v_cndmask_b32_e32 v4, v3, v10, vcc
	v_mad_u64_u32 v[4:5], s[2:3], v1, s2, v[4:5]
	v_and_b32_e32 v6, 48, v0
	v_mov_b32_e32 v7, v103
	v_ashrrev_i32_e32 v5, 31, v4
	v_lshl_add_u64 v[8:9], s[4:5], 0, v[6:7]
	v_lshlrev_b64 v[12:13], 6, v[4:5]
	v_lshl_add_u64 v[12:13], v[8:9], 0, v[12:13]
	global_load_dwordx4 v[46:49], v[12:13], off
	v_add_u32_e32 v12, 0xc8, v4
	v_ashrrev_i32_e32 v13, 31, v12
	v_lshlrev_b64 v[12:13], 6, v[12:13]
	v_lshl_add_u64 v[12:13], v[8:9], 0, v[12:13]
	global_load_dwordx4 v[50:53], v[12:13], off
	v_add_u32_e32 v12, 0x190, v4
	v_ashrrev_i32_e32 v13, 31, v12
	v_lshlrev_b64 v[12:13], 6, v[12:13]
	v_lshl_add_u64 v[12:13], v[8:9], 0, v[12:13]
	global_load_dwordx4 v[54:57], v[12:13], off
	v_add_u32_e32 v4, 0x258, v4
	v_ashrrev_i32_e32 v5, 31, v4
	v_lshlrev_b64 v[4:5], 6, v[4:5]
	v_lshl_add_u64 v[4:5], v[8:9], 0, v[4:5]
	global_load_dwordx4 v[58:61], v[4:5], off
	v_and_b32_e32 v13, 63, v0
	v_lshl_or_b32 v2, v2, 8, v13
	v_ashrrev_i32_e32 v3, 31, v2
	v_lshl_add_u64 v[2:3], v[2:3], 4, s[6:7]
	global_load_dwordx4 v[62:65], v[2:3], off
	global_load_dwordx4 v[66:69], v[2:3], off offset:1024
	global_load_dwordx4 v[70:73], v[2:3], off offset:2048
	global_load_dwordx4 v[74:77], v[2:3], off offset:3072
	v_bfe_u32 v12, v0, 6, 1
	v_lshl_add_u64 v[2:3], s[10:11], 0, v[6:7]
	v_and_b32_e32 v0, 64, v0
	v_cmp_gt_u32_e64 s[2:3], 16, v13
	s_waitcnt lgkmcnt(0)
	v_lshl_add_u64 v[4:5], s[12:13], 0, v[6:7]
	v_lshlrev_b32_e32 v6, 8, v12
	v_lshl_add_u64 v[104:105], v[2:3], 0, v[6:7]
	v_lshl_add_u64 v[106:107], v[4:5], 0, v[6:7]
	global_load_dwordx4 v[78:81], v[104:105], off
	global_load_dwordx4 v[82:85], v[104:105], off offset:64
	global_load_dwordx4 v[86:89], v[106:107], off
	global_load_dwordx4 v[90:93], v[106:107], off offset:64
	global_load_dwordx4 v[94:97], v[104:105], off offset:128
	global_load_dwordx4 v[6:9], v[104:105], off offset:192
	global_load_dwordx4 v[98:101], v[106:107], off offset:128
	global_load_dwordx4 v[2:5], v[106:107], off offset:192
	s_load_dword s6, s[14:15], 0x0
	s_waitcnt vmcnt(23)
	ds_write_b128 v102, v[14:17]
	s_waitcnt vmcnt(22)
	ds_write_b128 v102, v[18:21] offset:8192
	s_waitcnt vmcnt(21)
	ds_write_b128 v102, v[22:25] offset:16384
	s_waitcnt vmcnt(20)
	ds_write_b128 v102, v[26:29] offset:24576
	s_waitcnt vmcnt(19)
	ds_write_b128 v102, v[30:33] offset:32768
	s_waitcnt vmcnt(18)
	ds_write_b128 v102, v[34:37] offset:40960
	s_waitcnt vmcnt(17)
	ds_write_b128 v102, v[38:41] offset:49152
	s_waitcnt vmcnt(16)
	ds_write_b128 v102, v[42:45] offset:57344
	v_lshlrev_b32_e32 v14, 15, v12
	v_lshl_or_b32 v38, v13, 4, v14
	s_waitcnt lgkmcnt(0)
	s_barrier
	ds_read_b128 v[14:17], v38
	ds_read_b128 v[18:21], v38 offset:1024
	s_waitcnt vmcnt(15) lgkmcnt(1)
	v_mfma_f32_16x16x32_f16 v[14:17], v[14:17], v[46:49], 0
	ds_read_b128 v[22:25], v38 offset:2048
	ds_read_b128 v[26:29], v38 offset:10240
	ds_read_b128 v[30:33], v38 offset:18432
	s_waitcnt vmcnt(14) lgkmcnt(3)
	v_mfma_f32_16x16x32_f16 v[14:17], v[18:21], v[50:53], v[14:17]
	ds_read_b128 v[18:21], v38 offset:3072
	ds_read_b128 v[34:37], v38 offset:26624
	v_cmp_ne_u32_e64 s[4:5], 0, v0
	s_waitcnt vmcnt(13) lgkmcnt(4)
	v_mfma_f32_16x16x32_f16 v[14:17], v[22:25], v[54:57], v[14:17]
	ds_read_b128 v[22:25], v38 offset:4096
	s_and_b64 s[8:9], s[4:5], s[2:3]
	v_lshlrev_b32_e32 v0, 2, v108
	s_waitcnt vmcnt(12) lgkmcnt(2)
	v_mfma_f32_16x16x32_f16 v[14:17], v[18:21], v[58:61], v[14:17]
	ds_read_b128 v[18:21], v38 offset:5120
	s_waitcnt vmcnt(11) lgkmcnt(1)
	v_mfma_f32_16x16x32_f16 v[14:17], v[22:25], v[62:65], v[14:17]
	ds_read_b128 v[22:25], v38 offset:6144
	s_waitcnt vmcnt(10) lgkmcnt(1)
	v_mfma_f32_16x16x32_f16 v[14:17], v[18:21], v[66:69], v[14:17]
	ds_read_b128 v[18:21], v38 offset:7168
	s_waitcnt vmcnt(9) lgkmcnt(1)
	v_mfma_f32_16x16x32_f16 v[14:17], v[22:25], v[70:73], v[14:17]
	ds_read_b128 v[22:25], v38 offset:8192
	s_waitcnt vmcnt(8) lgkmcnt(1)
	v_mfma_f32_16x16x32_f16 v[14:17], v[18:21], v[74:77], v[14:17]
	ds_read_b128 v[18:21], v38 offset:9216
	s_waitcnt lgkmcnt(1)
	v_mfma_f32_16x16x32_f16 v[22:25], v[22:25], v[46:49], 0
	s_waitcnt vmcnt(7)
	s_nop 3
	v_add_f32_e32 v14, v14, v78
	v_mul_f32_e32 v14, 0x4038aa3b, v14
	v_add_f32_e32 v15, v15, v79
	s_waitcnt lgkmcnt(0)
	v_mfma_f32_16x16x32_f16 v[18:21], v[18:21], v[50:53], v[22:25]
	v_exp_f32_e32 v14, v14
	v_mul_f32_e32 v15, 0x4038aa3b, v15
	s_nop 0
	ds_read_b128 v[22:25], v38 offset:11264
	v_mfma_f32_16x16x32_f16 v[18:21], v[26:29], v[54:57], v[18:21]
	ds_read_b128 v[26:29], v38 offset:12288
	v_add_f32_e32 v16, v16, v80
	v_exp_f32_e32 v15, v15
	s_waitcnt lgkmcnt(1)
	v_mfma_f32_16x16x32_f16 v[18:21], v[22:25], v[58:61], v[18:21]
	ds_read_b128 v[22:25], v38 offset:13312
	v_mul_f32_e32 v16, 0x4038aa3b, v16
	v_add_f32_e32 v17, v17, v81
	s_waitcnt lgkmcnt(1)
	v_mfma_f32_16x16x32_f16 v[18:21], v[26:29], v[62:65], v[18:21]
	ds_read_b128 v[26:29], v38 offset:14336
	v_exp_f32_e32 v16, v16
	v_mul_f32_e32 v17, 0x4038aa3b, v17
	s_waitcnt lgkmcnt(1)
	v_mfma_f32_16x16x32_f16 v[18:21], v[22:25], v[66:69], v[18:21]
	ds_read_b128 v[22:25], v38 offset:15360
	v_exp_f32_e32 v17, v17
	v_add_f32_e32 v14, 1.0, v14
	s_waitcnt lgkmcnt(1)
	v_mfma_f32_16x16x32_f16 v[18:21], v[26:29], v[70:73], v[18:21]
	ds_read_b128 v[26:29], v38 offset:16384
	v_rcp_f32_e32 v14, v14
	v_add_f32_e32 v15, 1.0, v15
	s_waitcnt lgkmcnt(1)
	v_mfma_f32_16x16x32_f16 v[18:21], v[22:25], v[74:77], v[18:21]
	ds_read_b128 v[22:25], v38 offset:17408
	v_rcp_f32_e32 v15, v15
	v_add_f32_e32 v16, 1.0, v16
	s_waitcnt lgkmcnt(1)
	v_mfma_f32_16x16x32_f16 v[26:29], v[26:29], v[46:49], 0
	v_rcp_f32_e32 v16, v16
	v_add_f32_e32 v17, 1.0, v17
	v_rcp_f32_e32 v17, v17
	s_waitcnt lgkmcnt(0)
	v_mfma_f32_16x16x32_f16 v[22:25], v[22:25], v[50:53], v[26:29]
	v_fma_f32 v14, v14, -2.0, 1.0
	s_nop 1
	ds_read_b128 v[26:29], v38 offset:19456
	s_waitcnt vmcnt(5)
	v_fma_f32 v14, v14, v86, 0
	v_mfma_f32_16x16x32_f16 v[22:25], v[30:33], v[54:57], v[22:25]
	ds_read_b128 v[30:33], v38 offset:20480
	v_fma_f32 v15, v15, -2.0, 1.0
	v_fmac_f32_e32 v14, v15, v87
	s_waitcnt lgkmcnt(1)
	v_mfma_f32_16x16x32_f16 v[22:25], v[26:29], v[58:61], v[22:25]
	ds_read_b128 v[26:29], v38 offset:21504
	v_fma_f32 v15, v16, -2.0, 1.0
	v_fmac_f32_e32 v14, v15, v88
	s_waitcnt lgkmcnt(1)
	v_mfma_f32_16x16x32_f16 v[22:25], v[30:33], v[62:65], v[22:25]
	ds_read_b128 v[30:33], v38 offset:22528
	v_fma_f32 v15, v17, -2.0, 1.0
	v_add_f32_e32 v16, v18, v82
	s_waitcnt lgkmcnt(1)
	v_mfma_f32_16x16x32_f16 v[22:25], v[26:29], v[66:69], v[22:25]
	ds_read_b128 v[26:29], v38 offset:23552
	v_add_f32_e32 v17, v19, v83
	v_mul_f32_e32 v16, 0x4038aa3b, v16
	s_waitcnt lgkmcnt(1)
	v_mfma_f32_16x16x32_f16 v[22:25], v[30:33], v[70:73], v[22:25]
	ds_read_b128 v[30:33], v38 offset:24576
	v_mul_f32_e32 v17, 0x4038aa3b, v17
	v_exp_f32_e32 v16, v16
	s_waitcnt lgkmcnt(1)
	v_mfma_f32_16x16x32_f16 v[22:25], v[26:29], v[74:77], v[22:25]
	ds_read_b128 v[26:29], v38 offset:25600
	v_exp_f32_e32 v17, v17
	v_fmac_f32_e32 v14, v15, v89
	s_waitcnt lgkmcnt(1)
	v_mfma_f32_16x16x32_f16 v[30:33], v[30:33], v[46:49], 0
	v_add_f32_e32 v15, 1.0, v16
	v_add_f32_e32 v16, 1.0, v17
	v_add_f32_e32 v17, v20, v84
	s_waitcnt lgkmcnt(0)
	v_mfma_f32_16x16x32_f16 v[26:29], v[26:29], v[50:53], v[30:33]
	v_rcp_f32_e32 v15, v15
	s_nop 1
	ds_read_b128 v[30:33], v38 offset:27648
	v_mul_f32_e32 v17, 0x4038aa3b, v17
	v_mfma_f32_16x16x32_f16 v[26:29], v[34:37], v[54:57], v[26:29]
	ds_read_b128 v[34:37], v38 offset:28672
	v_rcp_f32_e32 v16, v16
	v_exp_f32_e32 v17, v17
	s_waitcnt lgkmcnt(1)
	v_mfma_f32_16x16x32_f16 v[26:29], v[30:33], v[58:61], v[26:29]
	ds_read_b128 v[30:33], v38 offset:29696
	v_fma_f32 v15, v15, -2.0, 1.0
	s_waitcnt vmcnt(4)
	v_fmac_f32_e32 v14, v15, v90
	v_fma_f32 v15, v16, -2.0, 1.0
	v_add_f32_e32 v16, 1.0, v17
	v_add_f32_e32 v17, v21, v85
	s_waitcnt lgkmcnt(1)
	v_mfma_f32_16x16x32_f16 v[26:29], v[34:37], v[62:65], v[26:29]
	ds_read_b128 v[34:37], v38 offset:30720
	v_rcp_f32_e32 v16, v16
	v_mul_f32_e32 v17, 0x4038aa3b, v17
	v_exp_f32_e32 v17, v17
	s_waitcnt lgkmcnt(1)
	v_mfma_f32_16x16x32_f16 v[26:29], v[30:33], v[66:69], v[26:29]
	ds_read_b128 v[30:33], v38 offset:31744
	v_fmac_f32_e32 v14, v15, v91
	v_fma_f32 v15, v16, -2.0, 1.0
	s_waitcnt vmcnt(3)
	v_add_f32_e32 v16, v22, v94
	v_fmac_f32_e32 v14, v15, v92
	v_add_f32_e32 v15, 1.0, v17
	v_mul_f32_e32 v16, 0x4038aa3b, v16
	v_add_f32_e32 v17, v23, v95
	v_exp_f32_e32 v16, v16
	v_mul_f32_e32 v17, 0x4038aa3b, v17
	v_exp_f32_e32 v17, v17
	s_waitcnt lgkmcnt(1)
	v_mfma_f32_16x16x32_f16 v[26:29], v[34:37], v[70:73], v[26:29]
	v_rcp_f32_e32 v15, v15
	v_add_f32_e32 v16, 1.0, v16
	v_rcp_f32_e32 v16, v16
	v_add_f32_e32 v17, 1.0, v17
	v_rcp_f32_e32 v17, v17
	s_waitcnt lgkmcnt(0)
	v_mfma_f32_16x16x32_f16 v[26:29], v[30:33], v[74:77], v[26:29]
	v_fma_f32 v15, v15, -2.0, 1.0
	v_fmac_f32_e32 v14, v15, v93
	v_fma_f32 v15, v16, -2.0, 1.0
	v_add_f32_e32 v16, v24, v96
	s_waitcnt vmcnt(1)
	v_fmac_f32_e32 v14, v15, v98
	v_fma_f32 v15, v17, -2.0, 1.0
	v_mul_f32_e32 v16, 0x4038aa3b, v16
	v_add_f32_e32 v17, v25, v97
	v_exp_f32_e32 v16, v16
	v_mul_f32_e32 v17, 0x4038aa3b, v17
	v_add_f32_e32 v6, v26, v6
	v_exp_f32_e32 v17, v17
	v_mul_f32_e32 v6, 0x4038aa3b, v6
	v_exp_f32_e32 v6, v6
	v_fmac_f32_e32 v14, v15, v99
	v_add_f32_e32 v15, 1.0, v16
	v_rcp_f32_e32 v15, v15
	v_add_f32_e32 v16, 1.0, v17
	v_rcp_f32_e32 v16, v16
	v_add_f32_e32 v6, 1.0, v6
	v_rcp_f32_e32 v6, v6
	v_add_f32_e32 v7, v27, v7
	v_mul_f32_e32 v7, 0x4038aa3b, v7
	v_fma_f32 v15, v15, -2.0, 1.0
	v_exp_f32_e32 v7, v7
	v_fmac_f32_e32 v14, v15, v100
	v_fma_f32 v15, v16, -2.0, 1.0
	v_fmac_f32_e32 v14, v15, v101
	v_fma_f32 v6, v6, -2.0, 1.0
	s_waitcnt vmcnt(0)
	v_fmac_f32_e32 v14, v6, v2
	v_add_f32_e32 v6, v28, v8
	v_add_f32_e32 v2, 1.0, v7
	v_mul_f32_e32 v6, 0x4038aa3b, v6
	v_add_f32_e32 v7, v29, v9
	v_exp_f32_e32 v6, v6
	v_mul_f32_e32 v7, 0x4038aa3b, v7
	v_exp_f32_e32 v7, v7
	v_rcp_f32_e32 v2, v2
	v_add_f32_e32 v6, 1.0, v6
	v_rcp_f32_e32 v6, v6
	v_add_f32_e32 v7, 1.0, v7
	v_rcp_f32_e32 v7, v7
	v_fma_f32 v2, v2, -2.0, 1.0
	v_fmac_f32_e32 v14, v2, v3
	v_fma_f32 v2, v6, -2.0, 1.0
	v_fmac_f32_e32 v14, v2, v4
	v_fma_f32 v2, v7, -2.0, 1.0
	v_fmac_f32_e32 v14, v2, v5
	v_mov_b32_e32 v2, v14
	s_nop 1
	v_permlane16_swap_b32_e32 v14, v2
	v_add_f32_e32 v2, v14, v2
	v_mov_b32_e32 v3, v2
	s_nop 1
	v_permlane32_swap_b32_e32 v2, v3
	v_add_f32_e32 v2, v2, v3
	s_and_saveexec_b64 s[4:5], s[8:9]
	v_lshl_or_b32 v3, v11, 6, v0
	v_add_u32_e32 v3, 0x10000, v3
	ds_write_b32 v3, v2
	s_or_b64 exec, exec, s[4:5]
	v_cmp_eq_u32_e64 s[4:5], 0, v12
	s_and_b64 s[2:3], s[4:5], s[2:3]
	s_and_b64 s[2:3], s[2:3], vcc
	s_waitcnt lgkmcnt(0)
	s_barrier
	s_and_saveexec_b64 s[4:5], s[2:3]
	s_cbranch_execz .LBB1_4
	v_lshl_or_b32 v0, v11, 6, v0
	v_add_u32_e32 v0, 0x10000, v0
	ds_read_b32 v0, v0
	s_movk_i32 s2, 0xc8
	s_waitcnt lgkmcnt(0)
	v_add_f32_e32 v0, v2, v0
	v_add_f32_e32 v0, s6, v0
	v_mul_f32_e32 v0, 0xbfb8aa3b, v0
	v_exp_f32_e32 v0, v0
	s_nop 0
	v_add_f32_e32 v0, 1.0, v0
	v_rcp_f32_e32 v2, v0
	v_mad_u64_u32 v[0:1], s[2:3], v1, s2, v[10:11]
	v_ashrrev_i32_e32 v1, 31, v0
	v_lshl_add_u64 v[0:1], v[0:1], 2, s[16:17]
	global_store_dword v[0:1], v2, off
